# v11: + P1 K-tile-t side-job finish/issue moved into the MFMA block (3-instruction chunks) (m1)
# speedup vs baseline: 1.0180x; 1.0040x over previous
;     __device__ __forceinline__ void finish(v4i_t& t0, v4i_t& t1, int j, int tid) const {
;         asm volatile("" : "+v"(t0), "+v"(t1));
;         const float* s0; unsigned char* d; addr(j, tid, s0, d);
;         const f32x4 r0 = __builtin_bit_cast(f32x4, t0) * 64.f, r1 = __builtin_bit_cast(f32x4, t1) * 64.f;
;         int w0 = 0, w1 = 0; w0 = __builtin_amdgcn_cvt_pk_fp8_f32(r0[0], r1[0], w0, false); w0 = __builtin_amdgcn_cvt_pk_fp8_f32(r0[1], r1[1], w0, true);
;         w1 = __builtin_amdgcn_cvt_pk_fp8_f32(r0[2], r1[2], w1, false); w1 = __builtin_amdgcn_cvt_pk_fp8_f32(r0[3], r1[3], w1, true);
;         typedef int v2is __attribute__((ext_vector_type(2))); __builtin_nontemporal_store((v2is){w0, w1}, (v2is*)d);
.Lp1vg_wd_a1:
	s_waitcnt lgkmcnt(0)
	s_barrier
	s_cmp_lt_i32 s98, 0
	s_cbranch_scc1 .Lp1vg_mmslow_a
	s_cmpk_gt_i32 s77, 0x5f
	s_cbranch_scc1 .Lp1vg_mmslow_a
	s_setprio 1
	s_waitcnt lgkmcnt(0)
	v_mfma_f32_16x16x32_bf16 v[138:141], v[158:161], v[198:201], v[138:141]
	s_add_i32 s4, s98, s68
	s_lshr_b32 s2, s4, 31
	s_add_i32 s2, s4, s2
	v_mfma_f32_16x16x32_bf16 v[134:137], v[166:169], v[198:201], v[134:137]
	s_ashr_i32 s5, s2, 1
	s_ashr_i32 s2, s2, 11
	s_and_b32 s3, s5, 0x3ff
	v_mfma_f32_16x16x32_bf16 v[122:125], v[158:161], v[190:193], v[122:125]
	s_ashr_i32 s56, s2, 31
	s_lshl_b32 s2, s2, 10
	v_pk_mul_f32 v[6:7], v[6:7], s[40:41] op_sel_hi:[1,0]
	v_mfma_f32_16x16x32_bf16 v[118:121], v[166:169], v[190:193], v[118:121]
	v_pk_mul_f32 v[8:9], v[8:9], s[40:41] op_sel_hi:[1,0]
	v_pk_mul_f32 v[10:11], v[10:11], s[40:41] op_sel_hi:[1,0]
	v_pk_mul_f32 v[12:13], v[12:13], s[40:41] op_sel_hi:[1,0]
	v_mfma_f32_16x16x32_bf16 v[106:109], v[158:161], v[182:185], v[106:109]
	s_or_b32 s2, s2, s3
	v_cvt_pk_fp8_f32 v6, v6, v10
	s_mul_hi_u32 s3, s2, 0x2100
	v_mfma_f32_16x16x32_bf16 v[102:105], v[166:169], v[182:185], v[102:105]
	s_mulk_i32 s56, 0x2100
	v_cvt_pk_fp8_f32 v6, v7, v11 op_sel:[0,0,1]
	s_add_i32 s3, s3, s56
	v_mfma_f32_16x16x32_bf16 v[90:93], v[158:161], v[174:177], v[90:93]
	s_mulk_i32 s2, 0x2100
	v_cvt_pk_fp8_f32 v7, v8, v12
	v_readlane_b32 s101, v251, 49
	v_mfma_f32_16x16x32_bf16 v[86:89], v[166:169], v[174:177], v[86:89]
	s_add_u32 s2, s101, s2
	v_readlane_b32 s101, v251, 31
	s_addc_u32 s3, s101, s3
	v_mfma_f32_16x16x32_bf16 v[138:141], v[162:165], v[202:205], v[138:141]
	v_cvt_pk_fp8_f32 v7, v9, v13 op_sel:[0,0,1]
	v_lshl_or_b32 v226, s4, 11, v208
	s_lshl_b32 s56, s5, 12
	v_mfma_f32_16x16x32_bf16 v[134:137], v[170:173], v[202:205], v[134:137]
	v_subrev_u32_e32 v4, s56, v226
	v_ashrrev_i32_e32 v5, 31, v4
	v_lshl_add_u64 v[4:5], v[4:5], 1, s[2:3]
	v_mfma_f32_16x16x32_bf16 v[122:125], v[162:165], v[194:197], v[122:125]
	global_store_dwordx2 v[4:5], v[6:7], off nt
	s_add_i32 s4, s77, s68
	s_lshr_b32 s2, s4, 31
	v_mfma_f32_16x16x32_bf16 v[118:121], v[170:173], v[194:197], v[118:121]
	s_add_i32 s2, s4, s2
	s_ashr_i32 s5, s2, 1
	s_ashr_i32 s2, s2, 11
	v_mfma_f32_16x16x32_bf16 v[106:109], v[162:165], v[186:189], v[106:109]
	s_ashr_i32 s3, s2, 31
	s_lshl_b64 s[2:3], s[2:3], 25
	v_readlane_b32 s82, v251, 36
	v_mfma_f32_16x16x32_bf16 v[102:105], v[170:173], v[186:189], v[102:105]
	v_readlane_b32 s83, v251, 37
	s_add_u32 s2, s82, s2
	s_addc_u32 s3, s83, s3
	v_mfma_f32_16x16x32_bf16 v[90:93], v[162:165], v[178:181], v[90:93]
	s_lshl_b32 s82, s5, 15
	s_and_b32 s82, s82, 0x1ff8000
	s_add_u32 s82, s2, s82
	s_addc_u32 s83, s3, 0
	v_mfma_f32_16x16x32_bf16 v[86:89], v[170:173], v[178:181], v[86:89]
	s_setprio 0
	s_setprio 1
	s_lshl_b32 s2, s5, 12
	s_lshl_b32 s3, s4, 11
	s_sub_i32 s2, s3, s2
	v_mfma_f32_16x16x32_bf16 v[130:133], v[142:145], v[198:201], v[130:133]
	s_ashr_i32 s3, s2, 31
	s_lshl_b64 s[2:3], s[2:3], 2
	s_add_u32 s2, s82, s2
	s_addc_u32 s3, s83, s3
	v_mfma_f32_16x16x32_bf16 v[126:129], v[150:153], v[198:201], v[126:129]
	v_lshlrev_b32_e32 v2, 2, v208
	v_lshl_add_u64 v[4:5], s[2:3], 0, v[2:3]
	v_lshl_add_u64 v[4:5], v[4:5], 0, s[42:43]
	v_mfma_f32_16x16x32_bf16 v[114:117], v[142:145], v[190:193], v[114:117]
	global_load_dwordx4 v[6:9], v2, s[2:3] nt
	global_load_dwordx4 v[10:13], v[4:5], off nt
	s_mov_b32 s100, 3
	v_mfma_f32_16x16x32_bf16 v[110:113], v[150:153], v[190:193], v[110:113]
	s_mov_b32 s98, s77
	s_add_i32 s77, s77, 1
	s_add_u32 s4, s54, 0xfff80080
	s_addc_u32 s5, s55, -1
	v_mfma_f32_16x16x32_bf16 v[98:101], v[142:145], v[182:185], v[98:101]
	s_cmp_eq_u32 s81, 28
	s_cselect_b32 s5, s7, s5
	s_cselect_b32 s4, s33, s4
	s_cselect_b32 s57, s45, s80
	s_cselect_b32 s56, s47, s79
	v_mfma_f32_16x16x32_bf16 v[94:97], v[150:153], v[182:185], v[94:97]
	v_mfma_f32_16x16x32_bf16 v[82:85], v[142:145], v[174:177], v[82:85]
	v_mfma_f32_16x16x32_bf16 v[78:81], v[150:153], v[174:177], v[78:81]
	v_mfma_f32_16x16x32_bf16 v[130:133], v[146:149], v[202:205], v[130:133]
	v_mfma_f32_16x16x32_bf16 v[126:129], v[154:157], v[202:205], v[126:129]
	v_mfma_f32_16x16x32_bf16 v[114:117], v[146:149], v[194:197], v[114:117]
	v_mfma_f32_16x16x32_bf16 v[110:113], v[154:157], v[194:197], v[110:113]
	v_mfma_f32_16x16x32_bf16 v[98:101], v[146:149], v[186:189], v[98:101]
	v_mfma_f32_16x16x32_bf16 v[94:97], v[154:157], v[186:189], v[94:97]
	v_mfma_f32_16x16x32_bf16 v[82:85], v[146:149], v[178:181], v[82:85]
	v_mfma_f32_16x16x32_bf16 v[78:81], v[154:157], v[178:181], v[78:81]
	s_setprio 0
	s_branch .Lp1vg_mmjoin_a
.Lp1vg_mmslow_a:
	s_mov_b32 s100, 0
	s_cmp_lt_i32 s98, 0
	s_cbranch_scc1 .Lp1vg_nf_a
	s_add_i32 s4, s98, s68
	s_lshr_b32 s2, s4, 31
	s_add_i32 s2, s4, s2
	s_ashr_i32 s5, s2, 1
	s_ashr_i32 s2, s2, 11
	s_and_b32 s3, s5, 0x3ff
	s_ashr_i32 s56, s2, 31
	s_lshl_b32 s2, s2, 10
	v_pk_mul_f32 v[6:7], v[6:7], s[40:41] op_sel_hi:[1,0]
	v_pk_mul_f32 v[8:9], v[8:9], s[40:41] op_sel_hi:[1,0]
	v_pk_mul_f32 v[10:11], v[10:11], s[40:41] op_sel_hi:[1,0]
	v_pk_mul_f32 v[12:13], v[12:13], s[40:41] op_sel_hi:[1,0]
	s_or_b32 s2, s2, s3
	v_cvt_pk_fp8_f32 v6, v6, v10
	s_mul_hi_u32 s3, s2, 0x2100
	s_mulk_i32 s56, 0x2100
	v_cvt_pk_fp8_f32 v6, v7, v11 op_sel:[0,0,1]
	s_add_i32 s3, s3, s56
	s_mulk_i32 s2, 0x2100
	v_cvt_pk_fp8_f32 v7, v8, v12
	v_readlane_b32 s101, v251, 49
	s_add_u32 s2, s101, s2
	v_readlane_b32 s101, v251, 31
	s_addc_u32 s3, s101, s3
	v_cvt_pk_fp8_f32 v7, v9, v13 op_sel:[0,0,1]
	v_lshl_or_b32 v226, s4, 11, v208
	s_lshl_b32 s56, s5, 12
	v_subrev_u32_e32 v4, s56, v226
	v_ashrrev_i32_e32 v5, 31, v4
	v_lshl_add_u64 v[4:5], v[4:5], 1, s[2:3]
	global_store_dwordx2 v[4:5], v[6:7], off nt
	s_mov_b32 s100, 1

.Lp1vg_ni_a:
	s_add_u32 s4, s54, 0xfff80080
	s_addc_u32 s5, s55, -1
	s_cmp_eq_u32 s81, 28
	s_cselect_b32 s5, s7, s5
	s_cselect_b32 s4, s33, s4
	s_cselect_b32 s57, s45, s80
	s_cselect_b32 s56, s47, s79
	s_setprio 1
	s_waitcnt lgkmcnt(0)
	v_mfma_f32_16x16x32_bf16 v[138:141], v[158:161], v[198:201], v[138:141]
	v_mfma_f32_16x16x32_bf16 v[134:137], v[166:169], v[198:201], v[134:137]
	v_mfma_f32_16x16x32_bf16 v[122:125], v[158:161], v[190:193], v[122:125]
	v_mfma_f32_16x16x32_bf16 v[118:121], v[166:169], v[190:193], v[118:121]
	v_mfma_f32_16x16x32_bf16 v[106:109], v[158:161], v[182:185], v[106:109]
	v_mfma_f32_16x16x32_bf16 v[102:105], v[166:169], v[182:185], v[102:105]
	v_mfma_f32_16x16x32_bf16 v[90:93], v[158:161], v[174:177], v[90:93]
	v_mfma_f32_16x16x32_bf16 v[86:89], v[166:169], v[174:177], v[86:89]
	v_mfma_f32_16x16x32_bf16 v[138:141], v[162:165], v[202:205], v[138:141]
	v_mfma_f32_16x16x32_bf16 v[134:137], v[170:173], v[202:205], v[134:137]
	v_mfma_f32_16x16x32_bf16 v[122:125], v[162:165], v[194:197], v[122:125]
	v_mfma_f32_16x16x32_bf16 v[118:121], v[170:173], v[194:197], v[118:121]
	v_mfma_f32_16x16x32_bf16 v[106:109], v[162:165], v[186:189], v[106:109]
	v_mfma_f32_16x16x32_bf16 v[102:105], v[170:173], v[186:189], v[102:105]
	v_mfma_f32_16x16x32_bf16 v[90:93], v[162:165], v[178:181], v[90:93]
	v_mfma_f32_16x16x32_bf16 v[86:89], v[170:173], v[178:181], v[86:89]
	s_setprio 0
	s_setprio 1
	v_mfma_f32_16x16x32_bf16 v[130:133], v[142:145], v[198:201], v[130:133]
	v_mfma_f32_16x16x32_bf16 v[126:129], v[150:153], v[198:201], v[126:129]
	v_mfma_f32_16x16x32_bf16 v[114:117], v[142:145], v[190:193], v[114:117]
	v_mfma_f32_16x16x32_bf16 v[110:113], v[150:153], v[190:193], v[110:113]
	v_mfma_f32_16x16x32_bf16 v[98:101], v[142:145], v[182:185], v[98:101]
	v_mfma_f32_16x16x32_bf16 v[94:97], v[150:153], v[182:185], v[94:97]
	v_mfma_f32_16x16x32_bf16 v[82:85], v[142:145], v[174:177], v[82:85]
	v_mfma_f32_16x16x32_bf16 v[78:81], v[150:153], v[174:177], v[78:81]
	v_mfma_f32_16x16x32_bf16 v[130:133], v[146:149], v[202:205], v[130:133]
	v_mfma_f32_16x16x32_bf16 v[126:129], v[154:157], v[202:205], v[126:129]
	v_mfma_f32_16x16x32_bf16 v[114:117], v[146:149], v[194:197], v[114:117]
	v_mfma_f32_16x16x32_bf16 v[110:113], v[154:157], v[194:197], v[110:113]
	v_mfma_f32_16x16x32_bf16 v[98:101], v[146:149], v[186:189], v[98:101]
	v_mfma_f32_16x16x32_bf16 v[94:97], v[154:157], v[186:189], v[94:97]
	v_mfma_f32_16x16x32_bf16 v[82:85], v[146:149], v[178:181], v[82:85]
	v_mfma_f32_16x16x32_bf16 v[78:81], v[154:157], v[178:181], v[78:81]
	s_setprio 0
.Lp1vg_mmjoin_a:
	s_barrier
	s_mov_b32 m0, s53
	v_lshl_add_u64 v[4:5], s[56:57], 0, v[212:213]
	s_add_u32 s82, s56, 0x80000
	ds_read_b128 v[174:177], v234 offset:16384
	ds_read_b128 v[178:181], v234 offset:17408
	ds_read_b128 v[182:185], v234 offset:18432
	ds_read_b128 v[186:189], v234 offset:19456
	ds_read_b128 v[190:193], v234 offset:20480
	ds_read_b128 v[194:197], v234 offset:21504
	ds_read_b128 v[198:201], v234 offset:22528
	ds_read_b128 v[202:205], v234 offset:23552
	global_load_lds_dwordx4 v[4:5], off
	v_lshl_add_u64 v[226:227], s[56:57], 0, v[216:217]
	s_mov_b32 m0, s60
	s_addc_u32 s83, s57, 0
	global_load_lds_dwordx4 v[226:227], off
	v_lshl_add_u64 v[228:229], s[82:83], 0, v[212:213]
	s_mov_b32 m0, s61
	v_lshl_add_u64 v[230:231], s[4:5], 0, v[214:215]
	global_load_lds_dwordx4 v[228:229], off
	v_lshl_add_u64 v[228:229], s[82:83], 0, v[216:217]
	s_mov_b32 m0, s64
	s_nop 0
	global_load_lds_dwordx4 v[228:229], off
	v_lshl_add_u64 v[228:229], s[4:5], 0, v[210:211]
	s_mov_b32 m0, s41
	s_nop 0
	global_load_lds_dwordx4 v[228:229], off
	s_mov_b32 m0, s65
	s_nop 0
	global_load_lds_dwordx4 v[230:231], off
	s_cmp_eq_u32 s100, 3
	s_cbranch_scc1 .Lp1vg_w11_a2
	s_waitcnt vmcnt(8)
	s_branch .Lp1vg_wd_a2
